# both GEMMs: K tile 1 staged before the first wait instead of after it (vmcnt 4 -> 10); gemm8 accumulator zeroing moved into that wait shadow
# speedup vs baseline: 1.0113x; 1.0113x over previous
.LBB5_2:
	s_or_b64 exec, exec, s[12:13]
	s_add_i32 s18, 0, 0x18000
	v_add_u32_e32 v60, s18, v18
	s_mov_b64 s[12:13], 0x100
	v_readfirstlane_b32 s19, v60
	v_add_u32_e32 v61, 0x2000, v60
	v_lshl_add_u64 v[2:3], v[2:3], 0, s[12:13]
	s_mov_b32 m0, s19
	v_readfirstlane_b32 s19, v61
	v_add_u32_e32 v62, 0x8000, v50
	global_load_lds_dwordx4 v[2:3], off
	v_lshl_add_u64 v[2:3], v[4:5], 0, s[12:13]
	s_mov_b32 m0, s19
	v_readfirstlane_b32 s19, v62
	v_add_u32_e32 v63, 0xa000, v50
	global_load_lds_dwordx4 v[2:3], off
	v_lshl_add_u64 v[2:3], v[6:7], 0, s[12:13]
	s_mov_b32 m0, s19
	v_readfirstlane_b32 s19, v63
	global_load_lds_dwordx4 v[2:3], off
	s_mov_b32 m0, s19
	s_add_i32 s19, 0, 0x1c000
	v_add_u32_e32 v64, s19, v18
	v_lshl_add_u64 v[2:3], v[8:9], 0, s[12:13]
	v_readfirstlane_b32 s20, v64
	global_load_lds_dwordx4 v[2:3], off
	v_lshl_add_u64 v[2:3], v[10:11], 0, s[12:13]
	s_mov_b32 m0, s20
	v_add_u32_e32 v66, 0x2000, v64
	global_load_lds_dwordx4 v[2:3], off
	v_lshl_add_u64 v[2:3], v[12:13], 0, s[12:13]
	v_readfirstlane_b32 s12, v66
	s_mov_b32 m0, s12
	v_lshlrev_b32_e32 v4, 2, v0
	global_load_lds_dwordx4 v[2:3], off
	s_waitcnt vmcnt(10)
	s_barrier
	v_lshlrev_b32_e32 v3, 6, v0
	v_and_b32_e32 v2, 48, v0
	v_and_b32_e32 v3, 0x3c0, v3
	v_and_b32_e32 v4, 32, v4
	s_and_b32 s12, s14, 7
	v_bitop3_b32 v2, v3, v4, v2 bitop3:0x36
	s_lshl_b32 s12, s12, 18
	s_load_dwordx2 s[0:1], s[0:1], 0x10
	s_mov_b32 s17, 0x18000
	v_add_u32_e32 v7, s15, v2
	v_add_u32_e32 v8, s16, v2
	v_add_u32_e32 v9, s18, v2
	v_add_u32_e32 v10, s19, v2
	v_add_u32_e32 v12, 0, v2
	v_lshlrev_b32_e32 v2, 3, v17
	v_lshlrev_b32_e32 v4, 11, v14
	s_add_u32 s4, s4, s12
	v_and_or_b32 v2, v2, s17, v4
	v_mov_b32_e32 v3, v39
	s_addc_u32 s5, s5, 0
	v_lshl_or_b32 v4, v1, 15, v4
	v_mov_b32_e32 v5, v39
	v_bfe_u32 v48, v0, 6, 2
	s_waitcnt vmcnt(6)
	v_lshl_add_u64 v[40:41], s[4:5], 0, v[2:3]
	v_lshl_add_u64 v[42:43], s[4:5], 0, v[4:5]
	s_add_u32 s4, s6, s10
	v_lshlrev_b32_e32 v6, 12, v48
	v_lshlrev_b32_e32 v11, 13, v1
	s_addc_u32 s5, s7, s11
	v_lshrrev_b32_e32 v49, 2, v0
	v_add_u32_e32 v38, v15, v16
	v_lshl_add_u64 v[44:45], s[4:5], 0, v[2:3]
	v_lshl_add_u64 v[46:47], s[4:5], 0, v[4:5]
	s_mov_b32 s16, -2
	v_add_u32_e32 v67, v7, v6
	v_add_u32_e32 v52, v12, v11
	s_mov_b64 s[4:5], 0x20100
	v_add_u32_e32 v65, v8, v6
	s_mov_b64 s[6:7], 0x200
	s_mov_b64 s[10:11], 0x20200
	v_add_u32_e32 v59, v9, v6
	s_mov_b64 s[12:13], 0x300
	s_mov_b64 s[14:15], 0x20300
	v_add_u32_e32 v54, v10, v6
	v_mov_b32_e32 v2, v39
	v_mov_b32_e32 v4, v39
	v_mov_b32_e32 v6, v39
	v_mov_b32_e32 v7, v39
	v_mov_b32_e32 v8, v39
	v_mov_b32_e32 v9, v39
	v_mov_b32_e32 v10, v39
	v_mov_b32_e32 v11, v39
	v_mov_b32_e32 v12, v39
	v_mov_b32_e32 v13, v39
	v_mov_b32_e32 v14, v39
	v_mov_b32_e32 v15, v39
	v_mov_b32_e32 v16, v39
	v_mov_b32_e32 v17, v39
	v_mov_b32_e32 v18, v39
	v_mov_b32_e32 v19, v39
	v_mov_b32_e32 v20, v39
	v_mov_b32_e32 v21, v39
	v_mov_b32_e32 v22, v39
	v_mov_b32_e32 v23, v39
	v_mov_b32_e32 v24, v39
	v_mov_b32_e32 v25, v39
	v_mov_b32_e32 v26, v39
	v_mov_b32_e32 v27, v39
	v_mov_b32_e32 v28, v39
	v_mov_b32_e32 v29, v39
	v_mov_b32_e32 v30, v39
	v_mov_b32_e32 v31, v39
	v_mov_b32_e32 v32, v39
	v_mov_b32_e32 v33, v39
	v_add_u32_e32 v68, 0xc000, v50
	v_add_u32_e32 v69, 0xe000, v50
	v_add_u32_e32 v70, 0x2000, v51
	v_add_u32_e32 v71, 0x2000, v55
	s_barrier

.LBB15_6:
	s_or_b64 exec, exec, s[8:9]
	s_add_i32 s27, 0, 0x18000
	v_add_u32_e32 v160, s27, v1
	s_load_dwordx4 s[8:11], s[0:1], 0x18
	s_mov_b64 s[0:1], 0x80
	v_readfirstlane_b32 s28, v160
	v_add_u32_e32 v161, 0x2000, v160
	v_lshl_add_u64 v[2:3], v[2:3], 0, s[0:1]
	s_mov_b32 m0, s28
	v_readfirstlane_b32 s28, v161
	v_add_u32_e32 v162, 0x8000, v153
	global_load_lds_dwordx4 v[2:3], off
	v_lshl_add_u64 v[2:3], v[4:5], 0, s[0:1]
	s_mov_b32 m0, s28
	v_readfirstlane_b32 s28, v162
	v_add_u32_e32 v163, 0xa000, v153
	global_load_lds_dwordx4 v[2:3], off
	v_lshl_add_u64 v[2:3], v[6:7], 0, s[0:1]
	s_mov_b32 m0, s28
	v_readfirstlane_b32 s28, v163
	global_load_lds_dwordx4 v[2:3], off
	s_mov_b32 m0, s28
	s_add_i32 s28, 0, 0x1c000
	v_add_u32_e32 v164, s28, v1
	v_lshl_add_u64 v[2:3], v[8:9], 0, s[0:1]
	v_readfirstlane_b32 s29, v164
	global_load_lds_dwordx4 v[2:3], off
	v_lshl_add_u64 v[2:3], v[10:11], 0, s[0:1]
	s_mov_b32 m0, s29
	v_add_u32_e32 v165, 0x2000, v164
	global_load_lds_dwordx4 v[2:3], off
	v_lshl_add_u64 v[2:3], v[12:13], 0, s[0:1]
	v_readfirstlane_b32 s0, v165
	s_mov_b32 m0, s0
	v_lshlrev_b32_e32 v4, 2, v0
	global_load_lds_dwordx4 v[2:3], off
	v_mov_b32_e32 v20, v131
	v_mov_b32_e32 v21, v131
	v_mov_b32_e32 v22, v131
	v_mov_b32_e32 v23, v131
	v_mov_b32_e32 v24, v131
	v_mov_b32_e32 v25, v131
	v_mov_b32_e32 v26, v131
	v_mov_b32_e32 v27, v131
	v_mov_b32_e32 v28, v131
	v_mov_b32_e32 v29, v131
	v_mov_b32_e32 v30, v131
	v_mov_b32_e32 v31, v131
	v_mov_b32_e32 v32, v131
	v_mov_b32_e32 v33, v131
	v_mov_b32_e32 v34, v131
	v_mov_b32_e32 v35, v131
	v_mov_b32_e32 v36, v131
	v_mov_b32_e32 v37, v131
	v_mov_b32_e32 v38, v131
	v_mov_b32_e32 v39, v131
	v_mov_b32_e32 v40, v131
	v_mov_b32_e32 v41, v131
	v_mov_b32_e32 v42, v131
	v_mov_b32_e32 v43, v131
	v_mov_b32_e32 v44, v131
	v_mov_b32_e32 v45, v131
	v_mov_b32_e32 v46, v131
	v_mov_b32_e32 v47, v131
	v_mov_b32_e32 v48, v131
	v_mov_b32_e32 v49, v131
	v_mov_b32_e32 v50, v131
	v_mov_b32_e32 v51, v131
	v_mov_b32_e32 v52, v131
	v_mov_b32_e32 v53, v131
	v_mov_b32_e32 v54, v131
	v_mov_b32_e32 v55, v131
	v_mov_b32_e32 v56, v131
	v_mov_b32_e32 v57, v131
	v_mov_b32_e32 v58, v131
	v_mov_b32_e32 v59, v131
	v_mov_b32_e32 v60, v131
	v_mov_b32_e32 v61, v131
	v_mov_b32_e32 v62, v131
	v_mov_b32_e32 v63, v131
	v_mov_b32_e32 v64, v131
	v_mov_b32_e32 v65, v131
	v_mov_b32_e32 v66, v131
	v_mov_b32_e32 v67, v131
	v_mov_b32_e32 v68, v131
	v_mov_b32_e32 v69, v131
	v_mov_b32_e32 v70, v131
	v_mov_b32_e32 v71, v131
	v_mov_b32_e32 v72, v131
	v_mov_b32_e32 v73, v131
	v_mov_b32_e32 v74, v131
	v_mov_b32_e32 v75, v131
	v_mov_b32_e32 v76, v131
	v_mov_b32_e32 v77, v131
	v_mov_b32_e32 v78, v131
	v_mov_b32_e32 v79, v131
	v_mov_b32_e32 v80, v131
	v_mov_b32_e32 v81, v131
	v_mov_b32_e32 v82, v131
	v_mov_b32_e32 v83, v131
	v_mov_b32_e32 v84, v131
	v_mov_b32_e32 v85, v131
	v_mov_b32_e32 v86, v131
	v_mov_b32_e32 v87, v131
	v_mov_b32_e32 v88, v131
	v_mov_b32_e32 v89, v131
	v_mov_b32_e32 v90, v131
	v_mov_b32_e32 v91, v131
	v_mov_b32_e32 v92, v131
	v_mov_b32_e32 v93, v131
	v_mov_b32_e32 v94, v131
	v_mov_b32_e32 v95, v131
	v_mov_b32_e32 v96, v131
	v_mov_b32_e32 v97, v131
	v_mov_b32_e32 v98, v131
	v_mov_b32_e32 v99, v131
	v_mov_b32_e32 v100, v131
	v_mov_b32_e32 v101, v131
	v_mov_b32_e32 v102, v131
	v_mov_b32_e32 v103, v131
	v_mov_b32_e32 v104, v131
	v_mov_b32_e32 v105, v131
	v_mov_b32_e32 v106, v131
	v_mov_b32_e32 v107, v131
	v_mov_b32_e32 v108, v131
	v_mov_b32_e32 v109, v131
	v_mov_b32_e32 v110, v131
	v_mov_b32_e32 v111, v131
	v_mov_b32_e32 v112, v131
	v_mov_b32_e32 v113, v131
	v_mov_b32_e32 v114, v131
	v_mov_b32_e32 v115, v131
	v_mov_b32_e32 v116, v131
	v_mov_b32_e32 v117, v131
	v_mov_b32_e32 v118, v131
	v_mov_b32_e32 v119, v131
	v_mov_b32_e32 v120, v131
	v_mov_b32_e32 v121, v131
	v_mov_b32_e32 v122, v131
	v_mov_b32_e32 v123, v131
	v_mov_b32_e32 v124, v131
	v_mov_b32_e32 v125, v131
	v_mov_b32_e32 v126, v131
	v_mov_b32_e32 v127, v131
	v_mov_b32_e32 v128, v131
	v_mov_b32_e32 v129, v131
	s_waitcnt vmcnt(10)
	s_barrier
	v_lshlrev_b32_e32 v3, 6, v0
	v_and_b32_e32 v2, 48, v0
	v_and_b32_e32 v3, 0x3c0, v3
	v_and_b32_e32 v4, 32, v4
	v_bitop3_b32 v2, v3, v4, v2 bitop3:0x36
	v_add_u32_e32 v7, s22, v2
	v_add_u32_e32 v8, s13, v2
	v_add_u32_e32 v9, s27, v2
	v_add_u32_e32 v10, s28, v2
	v_add_u32_e32 v12, 0, v2
	v_lshlrev_b32_e32 v2, 4, v17
	v_lshlrev_b32_e32 v4, 11, v14
	s_mov_b32 s0, 0x38000
	s_mov_b32 s26, 0x18000
	v_and_or_b32 v2, v2, s0, v4
	s_add_u32 s0, s23, s18
	v_lshlrev_b32_e32 v5, 8, v0
	v_mov_b32_e32 v3, v131
	s_addc_u32 s1, s7, s19
	v_and_or_b32 v4, v5, s26, v4
	v_mov_b32_e32 v5, v131
	v_bfe_u32 v147, v0, 6, 2
	s_waitcnt vmcnt(6)
	v_lshlrev_b32_e32 v11, 13, v145
	v_lshl_add_u64 v[136:137], s[0:1], 0, v[2:3]
	v_lshl_add_u64 v[138:139], s[0:1], 0, v[4:5]
	s_add_u32 s0, s21, s2
	v_lshlrev_b32_e32 v6, 12, v147
	v_or_b32_e32 v13, 0x800, v11
	v_or_b32_e32 v18, 0x1000, v11
	v_or_b32_e32 v19, 0x1800, v11
	s_addc_u32 s1, s20, s3
	v_add_u32_e32 v130, v15, v16
	v_lshl_add_u64 v[140:141], s[0:1], 0, v[2:3]
	v_lshl_add_u64 v[142:143], s[0:1], 0, v[4:5]
	s_mov_b32 s7, -2
	v_add_u32_e32 v167, v7, v6
	v_add_u32_e32 v151, v12, v11
	v_add_u32_e32 v150, v12, v13
	v_add_u32_e32 v149, v12, v18
	v_add_u32_e32 v148, v12, v19
	s_mov_b64 s[0:1], 0x40080
	s_mov_b64 s[2:3], 0x100
	s_mov_b64 s[18:19], 0x40100
	s_mov_b64 s[20:21], 0x180
	s_mov_b64 s[22:23], 0x40180
	v_add_u32_e32 v166, v8, v6
	v_add_u32_e32 v157, v9, v6
	v_add_u32_e32 v154, v10, v6
	v_mov_b32_e32 v2, v131
	v_mov_b32_e32 v4, v131
	v_mov_b32_e32 v6, v131
	v_mov_b32_e32 v7, v131
	v_mov_b32_e32 v8, v131
	v_mov_b32_e32 v9, v131
	v_mov_b32_e32 v10, v131
	v_mov_b32_e32 v11, v131
	v_mov_b32_e32 v12, v131
	v_mov_b32_e32 v13, v131
	v_mov_b32_e32 v14, v131
	v_mov_b32_e32 v15, v131
	v_mov_b32_e32 v16, v131
	v_mov_b32_e32 v17, v131
	v_mov_b32_e32 v18, v131
	v_mov_b32_e32 v19, v131
	v_and_b32_e32 v144, 15, v0
	v_lshlrev_b32_e32 v146, 6, v145
	v_add_u32_e32 v168, 0xc000, v153
	v_add_u32_e32 v169, 0xe000, v153
	v_add_u32_e32 v170, 0x2000, v152
	v_add_u32_e32 v171, 0x2000, v156
	s_barrier
